# layer-0 combine+LayerNorm row loop: gain/bias of the first two column groups resident in registers (v_fmac into bias -> v_fma with resident addend)
# speedup vs baseline: 1.0079x; 1.0027x over previous
; #define CMB_META(mm, M) do { const int _e0 = tok_e[2 * (mm)], _e1 = tok_e[2 * (mm) + 1]; (M).p0 = (size_t)pblk[_e0] * 256 + tok_p[2 * (mm)]; (M).p1 = (size_t)pblk[_e1] * 256 + tok_p[2 * (mm) + 1]; \
;         (M).h0 = tok_g[2 * (mm)] * (1.0f / 16.0f); (M).h1 = tok_g[2 * (mm) + 1] * (1.0f / 16.0f); } while (0)
; #define CMB_ROWS(mm, M, R) do { _Pragma("unroll") for (int i = 0; i < 4; ++i) { const int col = 8 * lane + 512 * i; (R).xa[i] = *(const u32x4*)(x1b + (size_t)(mm) * DM + col); \
;         (R).ya[i] = *(const u32x2*)((const unsigned char*)Yr + (M).p0 * DM + col); (R).yb[i] = *(const u32x2*)((const unsigned char*)Yr + (M).p1 * DM + col); } } while (0)
; #define CMB_PAIR(j, W, SEL) do { const f32x2 a2 = __builtin_amdgcn_cvt_pk_f32_fp8((int)aw[W], SEL), b2 = __builtin_amdgcn_cvt_pk_f32_fp8((int)bw[W], SEL); \
;                     v[i * 8 + 2 * (j)] = ALPHA * bflo(xw[j]) + h0 * a2[0] + h1 * b2[0]; v[i * 8 + 2 * (j) + 1] = ALPHA * bfhi(xw[j]) + h0 * a2[1] + h1 * b2[1]; \
;                     s += v[i * 8 + 2 * (j)] + v[i * 8 + 2 * (j) + 1]; } while (0)
; template <bool FINAL> ...
;     ...
;     const int mstep = G * 8, m0 = bid * 8 + wid;
;     Meta Mc, Mn; Rows Rc, Rn;
;     Mc.p0 = Mc.p1 = 0; Mc.h0 = Mc.h1 = 0.f; Mn = Mc;
;     if (m0 < T_) { CMB_META(m0, Mc); CMB_ROWS(m0, Mc, Rc); }
;     if (m0 + mstep < T_) CMB_META(m0 + mstep, Mn);
;     Rn = Rc;
;     for (int m = m0; m < T_; m += mstep) {
;         Meta Mnn = Mn;
;         if (m + mstep < T_) CMB_ROWS(m + mstep, Mn, Rn);
;         if (m + 2 * mstep < T_) CMB_META(m + 2 * mstep, Mnn);
;         const float h0 = Mc.h0, h1 = Mc.h1;
;         float v[32]; float s = 0.f;
; #pragma unroll
;         for (int i = 0; i < 4; ++i) {
;             const unsigned xw[4] = {Rc.xa[i].x, Rc.xa[i].y, Rc.xa[i].z, Rc.xa[i].w}; const unsigned aw[2] = {Rc.ya[i].x, Rc.ya[i].y}, bw[2] = {Rc.yb[i].x, Rc.yb[i].y};
;     ...
;             CMB_PAIR(0, 0, false); CMB_PAIR(1, 0, true); CMB_PAIR(2, 1, false); CMB_PAIR(3, 1, true);
;     ...
;         }
.LBB0_1104:
	s_andn2_b64 vcc, exec, s[6:7]
	s_cbranch_vccnz .LBB0_1111
	v_lshlrev_b32_e32 v232, 3, v4
	s_ashr_i32 s1, s0, 31
	v_lshl_add_u64 v[48:49], s[2:3], 0, v[232:233]
	s_lshl_b64 s[2:3], s[0:1], 11
	s_add_u32 s2, s40, s2
	s_addc_u32 s3, s41, s3
	v_lshl_add_u64 v[50:51], s[2:3], 0, v[232:233]
	s_lshl_b64 s[2:3], s[0:1], 12
	s_add_u32 s2, s42, s2
	v_readlane_b32 s1, v254, 50
	s_addc_u32 s3, s43, s3
	s_add_i32 s1, s1, s15
	s_lshl_b32 s34, s1, 1
	v_readlane_b32 s1, v254, 6
	s_add_i32 s6, s1, s15
	v_lshlrev_b32_e32 v6, 5, v4
	v_mov_b32_e32 v7, v233
	s_ashr_i32 s7, s6, 31
	v_lshl_add_u64 v[36:37], s[44:45], 0, v[6:7]
	v_lshl_add_u64 v[38:39], s[46:47], 0, v[6:7]
	v_or_b32_e32 v8, 0x1000, v6
	v_mov_b32_e32 v9, v233
	v_or_b32_e32 v6, 0x1800, v6
	s_lshl_b64 s[6:7], s[6:7], 12
	v_lshl_add_u64 v[40:41], s[44:45], 0, v[8:9]
	v_lshl_add_u64 v[42:43], s[46:47], 0, v[8:9]
	v_lshl_add_u64 v[44:45], s[44:45], 0, v[6:7]
	v_lshl_add_u64 v[46:47], s[46:47], 0, v[6:7]
	v_lshlrev_b32_e32 v232, 4, v4
	s_add_u32 s38, s42, s6
	s_waitcnt vmcnt(11)
	v_mov_b64_e32 v[4:5], v[32:33]
	s_waitcnt vmcnt(8)
	v_mov_b64_e32 v[8:9], v[28:29]
	s_waitcnt vmcnt(5)
	v_mov_b64_e32 v[12:13], v[24:25]
	s_waitcnt vmcnt(2)
	v_mov_b64_e32 v[16:17], v[20:21]
	s_addc_u32 s39, s43, s7
	v_mov_b64_e32 v[6:7], v[34:35]
	v_mov_b64_e32 v[10:11], v[30:31]
	v_mov_b64_e32 v[14:15], v[26:27]
	v_mov_b64_e32 v[18:19], v[22:23]
	v_mov_b64_e32 v[52:53], v[86:87]
	v_mov_b64_e32 v[54:55], v[82:83]
	v_mov_b64_e32 v[56:57], v[72:73]
	s_waitcnt vmcnt(1)
	v_mov_b64_e32 v[58:59], v[78:79]
	v_mov_b64_e32 v[60:61], v[88:89]
	v_mov_b64_e32 v[62:63], v[84:85]
	v_mov_b64_e32 v[64:65], v[74:75]
	s_waitcnt vmcnt(0)
	v_mov_b64_e32 v[68:69], v[80:81]
	global_load_dwordx4 v[176:179], v[36:37], off offset:16
	global_load_dwordx4 v[180:183], v[36:37], off
	global_load_dwordx4 v[184:187], v[38:39], off offset:16
	global_load_dwordx4 v[188:191], v[38:39], off
	global_load_dwordx4 v[192:195], v[36:37], off offset:2064
	global_load_dwordx4 v[196:199], v[36:37], off offset:2048
	global_load_dwordx4 v[200:203], v[38:39], off offset:2064
	global_load_dwordx4 v[212:215], v[38:39], off offset:2048
	s_branch .LBB0_1107
.LBB0_1106:
	v_cvt_pk_f32_fp8_e32 v[92:93], v86
	v_cvt_pk_f32_fp8_e32 v[94:95], v88
	v_lshlrev_b32_e32 v91, 16, v32
	v_and_b32_e32 v32, 0xffff0000, v32
	v_mov_b32_e32 v96, v92
	v_mov_b32_e32 v97, v94
	v_pk_mul_f32 v[96:97], v[76:77], v[96:97]
	v_mov_b32_e32 v94, v93
	v_fma_f32 v91, v90, v91, v96
	v_add_f32_e32 v91, v91, v97
	v_pk_mul_f32 v[92:93], v[76:77], v[94:95]
	v_cvt_pk_f32_fp8_sdwa v[94:95], v86 src0_sel:WORD_1
	v_cvt_pk_f32_fp8_sdwa v[96:97], v88 src0_sel:WORD_1
	v_fma_f32 v32, v90, v32, v92
	v_add_f32_e32 v92, v32, v93
	v_add_f32_e32 v32, v91, v92
	v_mov_b32_e32 v98, v94
	v_mov_b32_e32 v99, v96
	v_add_f32_e32 v93, 0, v32
	v_lshlrev_b32_e32 v32, 16, v33
	v_pk_mul_f32 v[98:99], v[76:77], v[98:99]
	v_mov_b32_e32 v96, v95
	v_fma_f32 v32, v90, v32, v98
	v_add_f32_e32 v86, v32, v99
	v_and_b32_e32 v88, 0xffff0000, v33
	v_pk_mul_f32 v[32:33], v[76:77], v[96:97]
	v_cvt_pk_f32_fp8_e32 v[94:95], v89
	v_fma_f32 v32, v90, v88, v32
	v_add_f32_e32 v88, v32, v33
	v_add_f32_e32 v32, v86, v88
	v_add_f32_e32 v98, v93, v32
	v_cvt_pk_f32_fp8_e32 v[32:33], v87
	v_mov_b32_e32 v97, v94
	v_lshlrev_b32_e32 v93, 16, v34
	v_and_b32_e32 v34, 0xffff0000, v34
	v_mov_b32_e32 v96, v32
	v_pk_mul_f32 v[96:97], v[76:77], v[96:97]
	v_mov_b32_e32 v94, v33
	v_fma_f32 v32, v90, v93, v96
	v_add_f32_e32 v93, v32, v97
	v_pk_mul_f32 v[32:33], v[76:77], v[94:95]
	v_cvt_pk_f32_fp8_sdwa v[96:97], v89 src0_sel:WORD_1
	v_fma_f32 v32, v90, v34, v32
	v_add_f32_e32 v95, v32, v33
	v_add_f32_e32 v32, v93, v95
	v_add_f32_e32 v34, v98, v32
	v_cvt_pk_f32_fp8_sdwa v[32:33], v87 src0_sel:WORD_1
	v_mov_b32_e32 v99, v96
	v_lshlrev_b32_e32 v87, 16, v35
	v_and_b32_e32 v35, 0xffff0000, v35
	v_mov_b32_e32 v98, v32
	v_pk_mul_f32 v[98:99], v[76:77], v[98:99]
	v_mov_b32_e32 v96, v33
	v_fma_f32 v32, v90, v87, v98
	v_add_f32_e32 v100, v32, v99
	v_pk_mul_f32 v[32:33], v[76:77], v[96:97]
	v_lshlrev_b32_e32 v89, 16, v28
	v_fma_f32 v32, v90, v35, v32
	v_add_f32_e32 v102, v32, v33
	v_add_f32_e32 v32, v100, v102
	v_add_f32_e32 v87, v34, v32
	v_cvt_pk_f32_fp8_e32 v[32:33], v82
	v_cvt_pk_f32_fp8_e32 v[34:35], v84
	v_and_b32_e32 v28, 0xffff0000, v28
	s_mov_b32 s0, 0x36600000
	v_mov_b32_e32 v96, v32
	v_mov_b32_e32 v97, v34
	v_mov_b32_e32 v34, v33
	v_pk_mul_f32 v[96:97], v[76:77], v[96:97]
	v_pk_mul_f32 v[34:35], v[76:77], v[34:35]
	v_fma_f32 v32, v90, v89, v96
	v_fma_f32 v28, v90, v28, v34
	v_add_f32_e32 v32, v32, v97
	v_add_f32_e32 v33, v28, v35
	v_cvt_pk_f32_fp8_sdwa v[34:35], v82 src0_sel:WORD_1
	v_cvt_pk_f32_fp8_sdwa v[96:97], v84 src0_sel:WORD_1
	v_add_f32_e32 v28, v32, v33
	v_add_f32_e32 v87, v87, v28
	v_mov_b32_e32 v98, v34
	v_mov_b32_e32 v99, v96
	v_lshlrev_b32_e32 v28, 16, v29
	v_pk_mul_f32 v[98:99], v[76:77], v[98:99]
	v_mov_b32_e32 v96, v35
	v_fma_f32 v28, v90, v28, v98
	v_add_f32_e32 v82, v28, v99
	v_and_b32_e32 v34, 0xffff0000, v29
	v_pk_mul_f32 v[28:29], v[76:77], v[96:97]
	s_nop 0
	v_fma_f32 v28, v90, v34, v28
	v_add_f32_e32 v84, v28, v29
	v_add_f32_e32 v28, v82, v84
	v_add_f32_e32 v94, v87, v28
	v_cvt_pk_f32_fp8_e32 v[28:29], v83
	v_cvt_pk_f32_fp8_e32 v[34:35], v85
	v_lshlrev_b32_e32 v87, 16, v30
	v_and_b32_e32 v30, 0xffff0000, v30
	v_mov_b32_e32 v96, v28
	v_mov_b32_e32 v97, v34
	v_pk_mul_f32 v[96:97], v[76:77], v[96:97]
	v_mov_b32_e32 v34, v29
	v_fma_f32 v28, v90, v87, v96
	v_add_f32_e32 v87, v28, v97
	v_pk_mul_f32 v[28:29], v[76:77], v[34:35]
	v_cvt_pk_f32_fp8_sdwa v[34:35], v85 src0_sel:WORD_1
	v_fma_f32 v28, v90, v30, v28
	v_add_f32_e32 v89, v28, v29
; #define CMB_PAIR(j, W, SEL) do { const f32x2 a2 = __builtin_amdgcn_cvt_pk_f32_fp8((int)aw[W], SEL), b2 = __builtin_amdgcn_cvt_pk_f32_fp8((int)bw[W], SEL); \
;                     v[i * 8 + 2 * (j)] = ALPHA * bflo(xw[j]) + h0 * a2[0] + h1 * b2[0]; v[i * 8 + 2 * (j) + 1] = ALPHA * bfhi(xw[j]) + h0 * a2[1] + h1 * b2[1]; \
;                     s += v[i * 8 + 2 * (j)] + v[i * 8 + 2 * (j) + 1]; } while (0)
; template <bool FINAL> ...
;     ...
;         for (int i = 0; i < 4; ++i) {
;             const unsigned xw[4] = {Rc.xa[i].x, Rc.xa[i].y, Rc.xa[i].z, Rc.xa[i].w}; const unsigned aw[2] = {Rc.ya[i].x, Rc.ya[i].y}, bw[2] = {Rc.yb[i].x, Rc.yb[i].y};
;     ...
;             CMB_PAIR(0, 0, false); CMB_PAIR(1, 0, true); CMB_PAIR(2, 1, false); CMB_PAIR(3, 1, true);
;     ...
;         }
;         Mc = Mn; Mn = Mnn; Rc = Rn;
;         const float mean = wave_sum(s) * (1.0f / DM); float q = 0.f;
	v_add_f32_e32 v28, v87, v89
	v_add_f32_e32 v30, v94, v28
	v_cvt_pk_f32_fp8_sdwa v[28:29], v83 src0_sel:WORD_1
	v_mov_b32_e32 v97, v34
	v_lshlrev_b32_e32 v83, 16, v31
	v_and_b32_e32 v31, 0xffff0000, v31
	v_mov_b32_e32 v96, v28
	v_pk_mul_f32 v[96:97], v[76:77], v[96:97]
	v_mov_b32_e32 v34, v29
	v_fma_f32 v28, v90, v83, v96
	v_add_f32_e32 v97, v28, v97
	v_pk_mul_f32 v[28:29], v[76:77], v[34:35]
	v_lshlrev_b32_e32 v85, 16, v24
	v_fma_f32 v28, v90, v31, v28
	v_add_f32_e32 v98, v28, v29
	v_add_f32_e32 v28, v97, v98
	v_add_f32_e32 v83, v30, v28
	v_cvt_pk_f32_fp8_e32 v[28:29], v72
	v_cvt_pk_f32_fp8_e32 v[30:31], v74
	v_and_b32_e32 v24, 0xffff0000, v24
	v_mov_b32_e32 v34, v28
	v_mov_b32_e32 v35, v30
	v_pk_mul_f32 v[34:35], v[76:77], v[34:35]
	v_mov_b32_e32 v30, v29
	v_fma_f32 v28, v90, v85, v34
	v_add_f32_e32 v34, v28, v35
	v_pk_mul_f32 v[28:29], v[76:77], v[30:31]
	v_cvt_pk_f32_fp8_sdwa v[30:31], v74 src0_sel:WORD_1
	v_fma_f32 v24, v90, v24, v28
	v_add_f32_e32 v35, v24, v29
	v_cvt_pk_f32_fp8_sdwa v[28:29], v72 src0_sel:WORD_1
	v_add_f32_e32 v24, v34, v35
	v_mov_b32_e32 v105, v30
	v_add_f32_e32 v85, v83, v24
	v_mov_b32_e32 v104, v28
	v_lshlrev_b32_e32 v24, 16, v25
	v_pk_mul_f32 v[104:105], v[76:77], v[104:105]
	v_mov_b32_e32 v30, v29
	v_fma_f32 v24, v90, v24, v104
	v_add_f32_e32 v74, v24, v105
	v_and_b32_e32 v28, 0xffff0000, v25
	v_pk_mul_f32 v[24:25], v[76:77], v[30:31]
	s_nop 0
	v_fma_f32 v24, v90, v28, v24
	v_add_f32_e32 v83, v24, v25
	v_add_f32_e32 v24, v74, v83
	v_add_f32_e32 v72, v85, v24
	v_cvt_pk_f32_fp8_e32 v[24:25], v73
	v_cvt_pk_f32_fp8_e32 v[28:29], v75
	v_lshlrev_b32_e32 v85, 16, v26
	v_and_b32_e32 v26, 0xffff0000, v26
	v_mov_b32_e32 v30, v24
	v_mov_b32_e32 v31, v28
	v_pk_mul_f32 v[30:31], v[76:77], v[30:31]
	v_mov_b32_e32 v28, v25
	v_fma_f32 v24, v90, v85, v30
	v_add_f32_e32 v85, v24, v31
	v_pk_mul_f32 v[24:25], v[76:77], v[28:29]
	v_cvt_pk_f32_fp8_sdwa v[28:29], v75 src0_sel:WORD_1
	v_fma_f32 v24, v90, v26, v24
	v_add_f32_e32 v94, v24, v25
	v_add_f32_e32 v24, v85, v94
	v_add_f32_e32 v26, v72, v24
	v_cvt_pk_f32_fp8_sdwa v[24:25], v73 src0_sel:WORD_1
	v_mov_b32_e32 v31, v28
	v_lshlrev_b32_e32 v72, 16, v27
	v_and_b32_e32 v27, 0xffff0000, v27
	v_mov_b32_e32 v30, v24
	v_pk_mul_f32 v[30:31], v[76:77], v[30:31]
	v_mov_b32_e32 v28, v25
	v_fma_f32 v24, v90, v72, v30
	v_add_f32_e32 v99, v24, v31
	v_pk_mul_f32 v[24:25], v[76:77], v[28:29]
	v_lshlrev_b32_e32 v31, 16, v20
	v_fma_f32 v24, v90, v27, v24
	v_add_f32_e32 v101, v24, v25
	v_add_f32_e32 v24, v99, v101
	v_add_f32_e32 v30, v26, v24
	v_cvt_pk_f32_fp8_e32 v[24:25], v78
	v_cvt_pk_f32_fp8_e32 v[26:27], v80
	v_and_b32_e32 v20, 0xffff0000, v20
	v_mov_b32_e32 v28, v24
	v_mov_b32_e32 v29, v26
	v_pk_mul_f32 v[28:29], v[76:77], v[28:29]
	v_mov_b32_e32 v26, v25
	v_fma_f32 v24, v90, v31, v28
	v_add_f32_e32 v72, v24, v29
	v_pk_mul_f32 v[24:25], v[76:77], v[26:27]
	v_cvt_pk_f32_fp8_sdwa v[26:27], v80 src0_sel:WORD_1
	v_fma_f32 v20, v90, v20, v24
	v_add_f32_e32 v73, v20, v25
	v_cvt_pk_f32_fp8_sdwa v[24:25], v78 src0_sel:WORD_1
	v_add_f32_e32 v20, v72, v73
	v_mov_b32_e32 v29, v26
	v_add_f32_e32 v30, v30, v20
	v_mov_b32_e32 v28, v24
	v_lshlrev_b32_e32 v20, 16, v21
	v_pk_mul_f32 v[28:29], v[76:77], v[28:29]
	v_mov_b32_e32 v26, v25
	v_fma_f32 v20, v90, v20, v28
	v_add_f32_e32 v75, v20, v29
	v_and_b32_e32 v24, 0xffff0000, v21
	v_pk_mul_f32 v[20:21], v[76:77], v[26:27]
	v_lshlrev_b32_e32 v29, 16, v22
	v_fma_f32 v20, v90, v24, v20
	v_add_f32_e32 v78, v20, v21
	v_add_f32_e32 v20, v75, v78
	v_add_f32_e32 v28, v30, v20
	v_cvt_pk_f32_fp8_e32 v[20:21], v79
	v_cvt_pk_f32_fp8_e32 v[24:25], v81
	v_and_b32_e32 v22, 0xffff0000, v22
	v_mov_b32_e32 v26, v20
	v_mov_b32_e32 v27, v24
	v_pk_mul_f32 v[26:27], v[76:77], v[26:27]
	v_mov_b32_e32 v24, v21
	v_fma_f32 v20, v90, v29, v26
	v_add_f32_e32 v80, v20, v27
	v_pk_mul_f32 v[20:21], v[76:77], v[24:25]
	v_cvt_pk_f32_fp8_sdwa v[24:25], v81 src0_sel:WORD_1
	v_fma_f32 v20, v90, v22, v20
	v_add_f32_e32 v96, v20, v21
	v_add_f32_e32 v20, v80, v96
	v_add_f32_e32 v22, v28, v20
	v_cvt_pk_f32_fp8_sdwa v[20:21], v79 src0_sel:WORD_1
	v_mov_b32_e32 v27, v24
	v_lshlrev_b32_e32 v28, 16, v23
	v_and_b32_e32 v23, 0xffff0000, v23
	v_mov_b32_e32 v26, v20
	v_pk_mul_f32 v[26:27], v[76:77], v[26:27]
	v_mov_b32_e32 v24, v21
	v_fma_f32 v20, v90, v28, v26
	v_add_f32_e32 v79, v20, v27
	v_pk_mul_f32 v[20:21], v[76:77], v[24:25]
	s_nop 0
	v_fma_f32 v20, v90, v23, v20
	v_add_f32_e32 v76, v20, v21
	v_add_f32_e32 v20, v79, v76
	v_add_f32_e32 v20, v22, v20
	ds_swizzle_b32 v21, v20 offset:swizzle(SWAP,1)
	s_waitcnt lgkmcnt(0)
	v_add_f32_e32 v20, v20, v21
	ds_swizzle_b32 v21, v20 offset:swizzle(SWAP,2)
	s_waitcnt lgkmcnt(0)
	v_add_f32_e32 v20, v20, v21
	ds_swizzle_b32 v21, v20 offset:swizzle(SWAP,4)
	s_waitcnt lgkmcnt(0)
	v_add_f32_e32 v20, v20, v21
	ds_swizzle_b32 v21, v20 offset:swizzle(SWAP,8)
	s_waitcnt lgkmcnt(0)
	v_add_f32_e32 v20, v20, v21
	ds_swizzle_b32 v21, v20 offset:swizzle(SWAP,16)
	s_waitcnt lgkmcnt(0)
; template <bool FINAL> ...
;     ...
;         const float mean = wave_sum(s) * (1.0f / DM); float q = 0.f;
; #pragma unroll
;         for (int i = 0; i < 32; ++i) { const float d = v[i] - mean; q += d * d; }
;         const float rstd = rsqrtf(wave_sum(q) * (1.0f / DM) + 1e-5f);
	v_add_f32_e32 v20, v20, v21
	v_mov_b32_e32 v21, v20
	s_nop 1
	v_permlane32_swap_b32_e32 v20, v21
	v_add_f32_e32 v20, v20, v21
	v_fmac_f32_e32 v92, 0xba000000, v20
	v_fmac_f32_e32 v91, 0xba000000, v20
	v_mul_f32_e32 v21, v92, v92
	v_fmac_f32_e32 v21, v91, v91
	v_fmac_f32_e32 v86, 0xba000000, v20
	v_fmac_f32_e32 v21, v86, v86
	v_fmac_f32_e32 v88, 0xba000000, v20
	v_fmac_f32_e32 v21, v88, v88
	v_fmac_f32_e32 v93, 0xba000000, v20
	v_fmac_f32_e32 v21, v93, v93
	v_fmac_f32_e32 v95, 0xba000000, v20
	v_fmac_f32_e32 v21, v95, v95
	v_fmac_f32_e32 v100, 0xba000000, v20
	v_fmac_f32_e32 v21, v100, v100
	v_fmac_f32_e32 v102, 0xba000000, v20
	v_fmac_f32_e32 v21, v102, v102
	v_fmac_f32_e32 v32, 0xba000000, v20
	v_fmac_f32_e32 v21, v32, v32
	v_fmac_f32_e32 v33, 0xba000000, v20
	v_fmac_f32_e32 v21, v33, v33
	v_fmac_f32_e32 v82, 0xba000000, v20
	v_fmac_f32_e32 v21, v82, v82
	v_fmac_f32_e32 v84, 0xba000000, v20
	v_fmac_f32_e32 v21, v84, v84
	v_fmac_f32_e32 v87, 0xba000000, v20
	v_fmac_f32_e32 v21, v87, v87
	v_fmac_f32_e32 v89, 0xba000000, v20
	v_fmac_f32_e32 v21, v89, v89
	v_fmac_f32_e32 v97, 0xba000000, v20
	v_fmac_f32_e32 v21, v97, v97
	v_fmac_f32_e32 v98, 0xba000000, v20
	v_fmac_f32_e32 v21, v98, v98
	v_fmac_f32_e32 v34, 0xba000000, v20
	v_fmac_f32_e32 v21, v34, v34
	v_fmac_f32_e32 v35, 0xba000000, v20
	v_fmac_f32_e32 v21, v35, v35
	v_fmac_f32_e32 v74, 0xba000000, v20
	v_fmac_f32_e32 v21, v74, v74
	v_fmac_f32_e32 v83, 0xba000000, v20
	v_fmac_f32_e32 v21, v83, v83
	v_fmac_f32_e32 v85, 0xba000000, v20
	v_fmac_f32_e32 v21, v85, v85
	v_fmac_f32_e32 v94, 0xba000000, v20
	v_fmac_f32_e32 v21, v94, v94
	v_fmac_f32_e32 v99, 0xba000000, v20
	v_fmac_f32_e32 v21, v99, v99
	v_fmac_f32_e32 v101, 0xba000000, v20
	v_fmac_f32_e32 v21, v101, v101
	v_fmac_f32_e32 v72, 0xba000000, v20
	v_fmac_f32_e32 v21, v72, v72
	v_fmac_f32_e32 v73, 0xba000000, v20
	v_fmac_f32_e32 v21, v73, v73
	v_fmac_f32_e32 v75, 0xba000000, v20
	v_fmac_f32_e32 v21, v75, v75
	v_fmac_f32_e32 v78, 0xba000000, v20
	v_fmac_f32_e32 v21, v78, v78
	v_fmac_f32_e32 v80, 0xba000000, v20
	v_fmac_f32_e32 v21, v80, v80
	v_fmac_f32_e32 v96, 0xba000000, v20
	v_fmac_f32_e32 v21, v96, v96
	v_fmac_f32_e32 v79, 0xba000000, v20
	v_fmac_f32_e32 v21, v79, v79
	v_fmac_f32_e32 v76, 0xba000000, v20
	v_fmac_f32_e32 v21, v76, v76
	ds_swizzle_b32 v20, v21 offset:swizzle(SWAP,1)
	s_waitcnt lgkmcnt(0)
	v_add_f32_e32 v20, v21, v20
	ds_swizzle_b32 v21, v20 offset:swizzle(SWAP,2)
	s_waitcnt lgkmcnt(0)
	v_add_f32_e32 v20, v20, v21
	ds_swizzle_b32 v21, v20 offset:swizzle(SWAP,4)
	s_waitcnt lgkmcnt(0)
	v_add_f32_e32 v20, v20, v21
	ds_swizzle_b32 v21, v20 offset:swizzle(SWAP,8)
	s_waitcnt lgkmcnt(0)
	v_add_f32_e32 v20, v20, v21
	ds_swizzle_b32 v21, v20 offset:swizzle(SWAP,16)
	s_waitcnt lgkmcnt(0)
	v_add_f32_e32 v20, v20, v21
	v_mov_b32_e32 v21, v20
	s_nop 1
	v_permlane32_swap_b32_e32 v20, v21
	v_add_f32_e32 v20, v20, v21
	v_mov_b32_e32 v21, 0x3727c5ac
	v_fmamk_f32 v20, v20, 0x3a000000, v21
	v_cmp_gt_f32_e32 vcc, s91, v20
	v_mul_f32_e32 v21, 0x4b800000, v20
	s_nop 0
	v_cndmask_b32_e32 v20, v20, v21, vcc
	v_rsq_f32_e32 v20, v20
	s_nop 0
	v_mul_f32_e32 v21, 0x45800000, v20
	v_cndmask_b32_e32 v77, v20, v21, vcc
	s_nop 0
	s_nop 0
	s_nop 0
	s_nop 0
	v_mul_f32_e32 v81, v91, v77
	v_mul_f32_e32 v34, v34, v77
	s_waitcnt vmcnt(0)
; __device__ __forceinline__ unsigned cvtpk(float lo, float hi) { unsigned r; asm volatile("v_cvt_pk_bf16_f32 %0, %1, %2" : "=v"(r) : "v"(lo), "v"(hi)); return r; }
; template <bool FINAL> ...
;     ...
; #pragma unroll
;         for (int i = 0; i < 4; ++i) { const int col = 8 * lane + 512 * i;
;             const f32x4 ga = *(const f32x4*)(g + col), gb = *(const f32x4*)(g + col + 4), ba = *(const f32x4*)(bb + col), bbv = *(const f32x4*)(bb + col + 4);
;             float y[8];
; #pragma unroll
;             for (int j = 0; j < 4; ++j) { y[j] = (v[i * 8 + j] - mean) * rstd * ga[j] + ba[j]; y[4 + j] = (v[i * 8 + 4 + j] - mean) * rstd * gb[j] + bbv[j]; }
;     ...
;             if (dbg_bad) { for (int j = 0; j < 8; ++j) y[j] = 0.f; }
;     ...
;             if constexpr (FINAL) { *(f32x4*)(fo + (size_t)m * DM + col) = (f32x4){y[0], y[1], y[2], y[3]}; *(f32x4*)(fo + (size_t)m * DM + col + 4) = (f32x4){y[4], y[5], y[6], y[7]}; }
;             else { *(u32x4*)(xo + (size_t)m * DM + col) = (u32x4){cvtpk(y[0], y[1]), cvtpk(y[2], y[3]), cvtpk(y[4], y[5]), cvtpk(y[6], y[7])};
;                 if constexpr (F8_IN) *(u32x2*)(xq + (size_t)m * DM + col) = (u32x2){pk4_fp8(y[0], y[1], y[2], y[3]), pk4_fp8(y[4], y[5], y[6], y[7])}; } }
	v_fma_f32 v108, v180, v81, v188
	v_mul_f32_e32 v28, v93, v77
	v_fma_f32 v109, v176, v28, v184
	v_mul_f32_e32 v20, v92, v77
	v_fma_f32 v28, v181, v20, v189
	v_mul_f32_e32 v20, v95, v77
	v_fma_f32 v29, v177, v20, v185
	v_mul_f32_e32 v20, v86, v77
	v_fma_f32 v30, v182, v20, v190
	v_mul_f32_e32 v20, v100, v77
	v_fma_f32 v26, v178, v20, v186
	v_mul_f32_e32 v20, v88, v77
	v_fma_f32 v31, v183, v20, v191
	v_mul_f32_e32 v20, v102, v77
	v_fma_f32 v27, v179, v20, v187
	v_cvt_pk_bf16_f32 v22, v108, v28
	v_cvt_pk_bf16_f32 v23, v30, v31
	v_cvt_pk_bf16_f32 v24, v109, v29
	v_cvt_pk_fp8_f32 v108, v108, v28
	v_cvt_pk_fp8_f32 v109, v109, v29
	v_lshl_add_u64 v[20:21], s[2:3], 0, v[232:233]
	v_add_co_u32_e32 v20, vcc, s0, v20
	v_cvt_pk_fp8_f32 v108, v30, v31 op_sel:[0,0,1]
	v_cvt_pk_fp8_f32 v109, v26, v27 op_sel:[0,0,1]
	v_addc_co_u32_e32 v21, vcc, 0, v21, vcc
	v_cvt_pk_bf16_f32 v25, v26, v27
	global_store_dwordx4 v[20:21], v[22:25], off
	global_store_dwordx2 v[50:51], v[108:109], off
	s_nop 0
	s_nop 0
	s_nop 0
	s_nop 0
	s_nop 0
	v_mul_f32_e32 v30, v32, v77
	v_readlane_b32 s0, v255, 29
	v_readlane_b32 s1, v255, 30
	v_fma_f32 v30, v30, v196, v212
	v_mul_f32_e32 v26, v87, v77
	v_fma_f32 v31, v26, v192, v200
	v_mul_f32_e32 v22, v33, v77
	v_fma_f32 v26, v22, v197, v213
	v_mul_f32_e32 v22, v89, v77
	v_fma_f32 v27, v22, v193, v201
	v_mul_f32_e32 v22, v82, v77
	v_fma_f32 v28, v22, v198, v214
	v_mul_f32_e32 v22, v97, v77
	v_fma_f32 v32, v22, v194, v202
	v_mul_f32_e32 v22, v84, v77
	v_fma_f32 v109, v22, v199, v215
	v_mul_f32_e32 v22, v98, v77
	v_fma_f32 v105, v22, v195, v203
	v_cvt_pk_bf16_f32 v22, v30, v26
	v_cvt_pk_bf16_f32 v23, v28, v109
	v_cvt_pk_bf16_f32 v24, v31, v27
	v_cvt_pk_fp8_f32 v30, v30, v26
	v_cvt_pk_fp8_f32 v31, v31, v27
	v_cvt_pk_bf16_f32 v25, v32, v105
	global_store_dwordx4 v[20:21], v[22:25], off offset:1024
	v_cvt_pk_fp8_f32 v30, v28, v109 op_sel:[0,0,1]
	v_cvt_pk_fp8_f32 v31, v32, v105 op_sel:[0,0,1]
	global_store_dwordx2 v[50:51], v[30:31], off offset:512
	global_load_dwordx4 v[22:25], v[40:41], off offset:16
	global_load_dwordx4 v[26:29], v[40:41], off
	s_nop 0
	global_load_dwordx4 v[30:33], v[42:43], off offset:16
	global_load_dwordx4 v[86:89], v[42:43], off
	s_waitcnt vmcnt(0)
	v_fma_f32 v84, v34, v26, v86
	v_mul_f32_e32 v26, v85, v77
	v_fma_f32 v85, v26, v22, v30
	v_mul_f32_e32 v22, v35, v77
	v_fma_f32 v26, v22, v27, v87
	v_mul_f32_e32 v22, v94, v77
	v_fma_f32 v27, v22, v23, v31
	v_mul_f32_e32 v22, v74, v77
	v_fma_f32 v28, v22, v28, v88
	v_mul_f32_e32 v22, v99, v77
	v_fma_f32 v30, v22, v24, v32
	v_mul_f32_e32 v22, v83, v77
	v_fmac_f32_e32 v89, v22, v29
	v_mul_f32_e32 v22, v101, v77
	v_fmac_f32_e32 v33, v22, v25
	v_cvt_pk_bf16_f32 v22, v84, v26
	v_cvt_pk_bf16_f32 v23, v28, v89
	v_cvt_pk_bf16_f32 v24, v85, v27
	v_cvt_pk_fp8_f32 v84, v84, v26
	v_cvt_pk_fp8_f32 v85, v85, v27
	v_cvt_pk_bf16_f32 v25, v30, v33
	global_store_dwordx4 v[20:21], v[22:25], off offset:2048
	v_cvt_pk_fp8_f32 v84, v28, v89 op_sel:[0,0,1]
	v_cvt_pk_fp8_f32 v85, v30, v33 op_sel:[0,0,1]
	v_mul_f32_e32 v34, v72, v77
	v_mov_b64_e32 v[86:87], v[52:53]
	v_mov_b64_e32 v[88:89], v[60:61]
	global_store_dwordx2 v[50:51], v[84:85], off offset:1024
	global_load_dwordx4 v[22:25], v[44:45], off offset:16
	global_load_dwordx4 v[26:29], v[44:45], off
	global_load_dwordx4 v[30:33], v[46:47], off offset:16
	s_nop 0
	global_load_dwordx4 v[82:85], v[46:47], off
	s_waitcnt vmcnt(0)
	v_fma_f32 v34, v34, v26, v82
	v_mul_f32_e32 v26, v80, v77
	v_fma_f32 v35, v26, v22, v30
	v_mul_f32_e32 v22, v73, v77
	v_fma_f32 v26, v22, v27, v83
	v_mul_f32_e32 v22, v96, v77
	v_fma_f32 v27, v22, v23, v31
	v_mul_f32_e32 v22, v75, v77
	v_fma_f32 v28, v22, v28, v84
	v_mul_f32_e32 v22, v79, v77
	v_fma_f32 v30, v22, v24, v32
	v_mul_f32_e32 v22, v78, v77
	v_fmac_f32_e32 v85, v22, v29
	v_mul_f32_e32 v22, v76, v77
	v_fmac_f32_e32 v33, v22, v25
	v_cvt_pk_bf16_f32 v22, v34, v26
	v_cvt_pk_bf16_f32 v23, v28, v85
	v_cvt_pk_bf16_f32 v24, v35, v27
	v_cvt_pk_fp8_f32 v34, v34, v26
	v_cvt_pk_fp8_f32 v35, v35, v27
	v_cvt_pk_bf16_f32 v25, v30, v33
	global_store_dwordx4 v[20:21], v[22:25], off offset:3072
	v_cvt_pk_fp8_f32 v34, v28, v85 op_sel:[0,0,1]
	v_cvt_pk_fp8_f32 v35, v30, v33 op_sel:[0,0,1]
	v_mov_b64_e32 v[30:31], v[10:11]
	v_mov_b64_e32 v[26:27], v[14:15]
	v_mov_b64_e32 v[22:23], v[18:19]
	global_store_dwordx2 v[50:51], v[34:35], off offset:1536
	v_lshl_add_u64 v[50:51], v[50:51], 0, s[0:1]
	v_readlane_b32 s0, v255, 25
	v_readlane_b32 s1, v255, 26
	s_add_u32 s2, s2, s0
	s_addc_u32 s3, s3, s1
	s_add_i32 s34, s34, s80
	s_add_u32 s38, s38, s0
	v_mov_b64_e32 v[34:35], v[6:7]
	s_addc_u32 s39, s39, s1
	s_and_b64 vcc, exec, s[40:41]
	v_mov_b64_e32 v[32:33], v[4:5]
	v_mov_b64_e32 v[28:29], v[8:9]
	v_mov_b64_e32 v[24:25], v[12:13]
	v_mov_b64_e32 v[20:21], v[16:17]
	v_mov_b64_e32 v[82:83], v[54:55]
	v_mov_b64_e32 v[72:73], v[56:57]
	v_mov_b64_e32 v[78:79], v[58:59]
	v_mov_b64_e32 v[84:85], v[62:63]
	v_mov_b64_e32 v[74:75], v[64:65]
	v_mov_b64_e32 v[80:81], v[68:69]
	s_mov_b32 s0, s6
	v_mov_b64_e32 v[76:77], v[66:67]
	s_cbranch_vccnz .LBB0_1111
